# speedup vs baseline: 1.0176x; 1.0147x over previous
_Z8knn_gemmPKcS0_Pi:
	s_ashr_i32 s3, s2, 31
	s_lshr_b32 s3, s3, 29
	s_add_i32 s3, s2, s3
	s_ashr_i32 s4, s3, 3
	s_and_b32 s3, s3, -8
	s_sub_i32 s3, s2, s3
	s_cmp_lt_i32 s3, 0
	s_movk_i32 s12, 0x188
	s_cselect_b32 s5, s12, 0x187
	s_mul_i32 s3, s5, s3
	s_add_i32 s3, s3, s4
	s_ashr_i32 s4, s3, 31
	s_lshr_b32 s4, s4, 27
	s_add_i32 s10, s3, s4
	s_ashr_i32 s4, s10, 5
	s_lshl_b32 s11, s4, 2
	s_sub_i32 s4, 0x187, s11
	s_min_i32 s13, s4, 4
	s_abs_i32 s14, s13
	v_cvt_f32_u32_e32 v1, s14
	s_andn2_b32 s10, s10, 31
	s_load_dwordx4 s[4:7], s[0:1], 0x0
	s_load_dwordx2 s[8:9], s[0:1], 0x10
	s_sub_i32 s0, s3, s10
	v_rcp_iflag_f32_e32 v1, v1
	s_sub_i32 s10, 0, s14
	s_abs_i32 s3, s0
	s_xor_b32 s1, s0, s13
	v_mul_f32_e32 v1, 0x4f7ffffe, v1
	v_cvt_u32_f32_e32 v1, v1
	s_ashr_i32 s1, s1, 31
	v_lshrrev_b32_e32 v2, 8, v0
	v_lshlrev_b32_e32 v168, 4, v0
	v_readfirstlane_b32 s15, v1
	s_mul_i32 s10, s10, s15
	s_mul_hi_u32 s10, s15, s10
	s_add_i32 s15, s15, s10
	s_mul_hi_u32 s10, s3, s15
	s_mul_i32 s15, s10, s14
	s_sub_i32 s3, s3, s15
	s_add_i32 s15, s10, 1
	s_sub_i32 s16, s3, s14
	s_cmp_ge_u32 s3, s14
	s_cselect_b32 s10, s15, s10
	s_cselect_b32 s3, s16, s3
	s_add_i32 s15, s10, 1
	s_cmp_ge_u32 s3, s14
	s_cselect_b32 s3, s15, s10
	s_xor_b32 s3, s3, s1
	s_sub_i32 s34, s3, s1
	s_mul_i32 s1, s34, s13
	s_sub_i32 s0, s0, s1
	s_add_i32 s11, s11, s0
	v_readfirstlane_b32 s1, v0
	s_sub_i32 s13, 0x186, s11
	s_lshl_b32 s3, s1, 4
	s_mul_i32 s10, s34, 0x30000
	s_mul_hi_i32 s1, s34, 0x30000
	s_waitcnt lgkmcnt(0)
	s_add_u32 s10, s6, s10
	s_addc_u32 s11, s7, s1
	s_mul_i32 s14, s13, 0x30000
	s_mul_hi_i32 s1, s13, 0x30000
	s_add_u32 s22, s4, s14
	v_readfirstlane_b32 s0, v2
	s_addc_u32 s23, s5, s1
	s_cmp_eq_u32 s0, 0
	s_cselect_b64 s[0:1], -1, 0
	s_add_u32 s16, s10, 0x2000
	s_addc_u32 s17, s11, 0
	s_add_u32 s18, s22, 0xfffff000
	s_addc_u32 s19, s23, -1
	s_and_b64 s[14:15], s[0:1], exec
	s_cselect_b32 s17, s17, s19
	s_cselect_b32 s16, s16, s18
	s_add_u32 s18, s22, 0x1000
	s_addc_u32 s19, s23, 0
	s_add_i32 s14, s3, 0
	s_mov_b64 s[20:21], s[10:11]
	s_add_i32 s15, s14, 0x2000
	v_lshrrev_b32_e32 v5, 2, v0
	v_lshrrev_b32_e32 v1, 4, v0
	s_add_i32 s16, s14, 0x4000
	v_and_b32_e32 v5, 2, v5
	s_add_u32 s18, s10, 0x3000
	s_addc_u32 s19, s11, 0
	s_add_u32 s3, s10, 0x5000
	s_addc_u32 s17, s11, 0
	s_add_u32 s20, s22, 0x2000
	s_addc_u32 s21, s23, 0
	s_and_b64 s[10:11], s[0:1], exec
	s_cselect_b32 s11, s17, s21
	s_cselect_b32 s10, s3, s20
	s_add_u32 s20, s22, 0x4000
	s_addc_u32 s21, s23, 0
	s_add_i32 s17, s14, 0x6000
	v_add_lshl_u32 v1, v5, v1, 3
	s_add_i32 s18, s14, 0x8000
	s_add_i32 s19, s14, 0xa000
	v_and_b32_e32 v3, 15, v0
	v_and_b32_e32 v5, 24, v1
	v_lshrrev_b32_e32 v1, 1, v0
	s_movk_i32 s3, 0x60
	s_add_i32 s20, s14, 0xc000
	v_and_or_b32 v1, v1, s3, v3
	v_lshl_or_b32 v2, v2, 6, v3
	s_add_u32 s21, s4, 0x12000
	v_and_b32_e32 v4, 48, v0
	v_mad_u32_u24 v6, v1, s3, 0
	v_mad_u32_u24 v2, v2, s3, 0
	s_addc_u32 s22, s5, 0
	v_add_u32_e32 v1, v6, v4
	v_add_u32_e32 v170, v2, v4
	v_add_u32_e32 v172, v6, v5
	v_add_u32_e32 v173, v2, v5
	v_mov_b32_e32 v39, 0
	s_add_u32 s23, s6, 0x12000
	v_add_u32_e32 v171, 0x3000, v170
	v_add_u32_e32 v174, 0x3040, v173
	v_mov_b32_e32 v169, v39
	v_add_u32_e32 v175, 0x12000, v1
	v_add_u32_e32 v176, 0x12040, v172
	v_add_u32_e32 v177, 0x15000, v170
	v_add_u32_e32 v178, 0x15040, v173
	v_add_u32_e32 v179, 0x12600, v1
	v_add_u32_e32 v180, 0x12640, v172
	v_add_u32_e32 v181, 0x15600, v170
	v_add_u32_e32 v182, 0x15640, v173
	v_add_u32_e32 v183, 0x15c00, v170
	v_add_u32_e32 v184, 0x15c40, v173
	v_add_u32_e32 v185, 0x16200, v170
	v_add_u32_e32 v186, 0x16240, v173
	s_addc_u32 s24, s7, 0
	v_mov_b32_e32 v187, 0x7f7f7f7f
	s_add_i32 s25, 0, 0x18000
	s_movk_i32 s26, 0xff80
	s_movk_i32 s27, 0x30e
	s_add_i32 s28, s14, 0xe000
	s_add_i32 s29, s20, 0x4000
	s_add_i32 s30, s14, 0x12000
	s_add_i32 s31, s14, 0x14000
	s_add_i32 s33, s14, 0x16000
	s_lshr_b32 s66, s14, 12
	s_and_b32 s54, s14, 0xfff
	s_mul_i32 s67, s66, 0x6000
	s_add_i32 s54, s54, s67
	s_add_i32 s55, s54, 0x1000
	s_add_i32 s56, s54, 0x2000
	s_add_i32 s57, s54, 0x3000
	s_add_i32 s58, s54, 0x4000
	s_add_i32 s59, s54, 0x5000
	s_add_i32 s60, s54, 0xc000
	s_add_i32 s61, s54, 0xd000
	s_add_i32 s62, s54, 0xe000
	s_add_i32 s63, s54, 0xf000
	s_add_i32 s64, s54, 0x10000
	s_add_i32 s65, s54, 0x11000
	v_and_b32_e32 v228, 0xfff, v168
	v_add_u32_e32 v229, 0x1000, v228
	v_add_u32_e32 v230, 0x2000, v228
	s_mul_i32 s68, s34, 0x30000
	s_mul_hi_i32 s69, s34, 0x30000
	s_add_u32 s68, s6, s68
	s_addc_u32 s69, s7, s69
	s_mul_i32 s70, s13, 0x30000
	s_mul_hi_i32 s71, s13, 0x30000
	s_add_u32 s70, s4, s70
	s_addc_u32 s71, s5, s71
	s_mul_i32 s67, s66, 0x3000
	s_add_u32 s68, s68, s67
	s_addc_u32 s69, s69, 0
	s_add_u32 s70, s70, s67
	s_addc_u32 s71, s71, 0
	s_mov_b32 m0, s54
	s_nop 0
	global_load_lds_dwordx4 v228, s[68:69]
	s_mov_b32 m0, s55
	s_nop 0
	global_load_lds_dwordx4 v229, s[68:69]
	s_mov_b32 m0, s56
	s_nop 0
	global_load_lds_dwordx4 v230, s[68:69]
	s_mov_b32 m0, s57
	s_nop 0
	global_load_lds_dwordx4 v228, s[70:71]
	s_mov_b32 m0, s58
	s_nop 0
	global_load_lds_dwordx4 v229, s[70:71]
	s_mov_b32 m0, s59
	s_nop 0
	global_load_lds_dwordx4 v230, s[70:71]
	s_waitcnt vmcnt(0)
	s_barrier
	s_add_u32 s68, s68, 0x6000
	s_addc_u32 s69, s69, 0
	s_add_u32 s70, s70, 0x6000
	s_addc_u32 s71, s71, 0
	s_mov_b32 m0, s60
	s_nop 0
	global_load_lds_dwordx4 v228, s[68:69]
	s_mov_b32 m0, s61
	s_nop 0
	global_load_lds_dwordx4 v229, s[68:69]
	s_mov_b32 m0, s62
	s_nop 0
	global_load_lds_dwordx4 v230, s[68:69]
	s_mov_b32 m0, s63
	s_nop 0
	global_load_lds_dwordx4 v228, s[70:71]
	s_mov_b32 m0, s64
	s_nop 0
	global_load_lds_dwordx4 v229, s[70:71]
	s_mov_b32 m0, s65
	s_nop 0
	global_load_lds_dwordx4 v230, s[70:71]
	s_branch .LBB1_2
.LBB1_1:
	v_and_b32_e32 v8, 0xffffff80, v164
	v_and_or_b32 v9, v165, s26, 1
	v_max_i32_e32 v10, v8, v9
	v_min_i32_e32 v11, v8, v9
	v_and_or_b32 v12, v166, s26, 2
	v_max_i32_e32 v10, v10, v12
	v_med3_i32 v8, v8, v9, v12
	v_min_i32_e32 v9, v11, v12
	v_and_or_b32 v11, v167, s26, 3
	v_max_i32_e32 v12, v10, v11
	v_med3_i32 v10, v10, v8, v11
	v_min_i32_e32 v8, v8, v11
	v_max_i32_e32 v8, v9, v8
	v_and_or_b32 v9, v160, s26, 4
	v_max_i32_e32 v11, v12, v9
	v_med3_i32 v12, v12, v10, v9
	v_med3_i32 v8, v10, v8, v9
	v_and_or_b32 v9, v161, s26, 5
	v_max_i32_e32 v10, v11, v9
	v_med3_i32 v11, v11, v12, v9
	v_med3_i32 v8, v12, v8, v9
	v_and_or_b32 v9, v162, s26, 6
	v_max_i32_e32 v12, v10, v9
	v_med3_i32 v10, v10, v11, v9
	v_med3_i32 v8, v11, v8, v9
	v_and_or_b32 v9, v163, s26, 7
	v_max_i32_e32 v11, v12, v9
	v_med3_i32 v12, v12, v10, v9
	v_med3_i32 v8, v10, v8, v9
	v_and_or_b32 v9, v156, s26, 8
	v_max_i32_e32 v10, v11, v9
	v_med3_i32 v11, v11, v12, v9
	v_med3_i32 v8, v12, v8, v9
	v_and_or_b32 v9, v157, s26, 9
	v_max_i32_e32 v12, v10, v9
	v_med3_i32 v10, v10, v11, v9
	v_med3_i32 v8, v11, v8, v9
	v_and_or_b32 v9, v158, s26, 10
	v_max_i32_e32 v11, v12, v9
	v_med3_i32 v12, v12, v10, v9
	v_med3_i32 v8, v10, v8, v9
	v_and_or_b32 v9, v159, s26, 11
	v_max_i32_e32 v10, v11, v9
	v_med3_i32 v11, v11, v12, v9
	v_med3_i32 v8, v12, v8, v9
	v_and_or_b32 v9, v152, s26, 12
	v_max_i32_e32 v12, v10, v9
	v_med3_i32 v10, v10, v11, v9
	v_med3_i32 v8, v11, v8, v9
	v_and_or_b32 v9, v153, s26, 13
	v_max_i32_e32 v11, v12, v9
	v_med3_i32 v12, v12, v10, v9
	v_med3_i32 v8, v10, v8, v9
	v_and_or_b32 v9, v154, s26, 14
	v_max_i32_e32 v10, v11, v9
	v_med3_i32 v11, v11, v12, v9
	v_med3_i32 v8, v12, v8, v9
	v_and_or_b32 v9, v155, s26, 15
	v_max_i32_e32 v12, v10, v9
	v_med3_i32 v10, v10, v11, v9
	v_med3_i32 v8, v11, v8, v9
	v_and_or_b32 v9, v144, s26, 16
	v_max_i32_e32 v11, v12, v9
	v_med3_i32 v12, v12, v10, v9
	v_med3_i32 v8, v10, v8, v9
	v_and_or_b32 v9, v145, s26, 17
	v_max_i32_e32 v10, v11, v9
	v_med3_i32 v11, v11, v12, v9
	v_med3_i32 v8, v12, v8, v9
	v_and_or_b32 v9, v146, s26, 18
	v_max_i32_e32 v12, v10, v9
	v_med3_i32 v10, v10, v11, v9
	v_med3_i32 v8, v11, v8, v9
	v_and_or_b32 v9, v147, s26, 19
	v_max_i32_e32 v11, v12, v9
	v_med3_i32 v12, v12, v10, v9
	v_med3_i32 v8, v10, v8, v9
	v_and_or_b32 v9, v136, s26, 20
	v_max_i32_e32 v10, v11, v9
	v_med3_i32 v11, v11, v12, v9
	v_med3_i32 v8, v12, v8, v9
	v_and_or_b32 v9, v137, s26, 21
	v_max_i32_e32 v12, v10, v9
	v_med3_i32 v10, v10, v11, v9
	v_med3_i32 v8, v11, v8, v9
	v_and_or_b32 v9, v138, s26, 22
	v_max_i32_e32 v11, v12, v9
	v_med3_i32 v12, v12, v10, v9
	v_med3_i32 v8, v10, v8, v9
	v_and_or_b32 v9, v139, s26, 23
	v_max_i32_e32 v10, v11, v9
	v_med3_i32 v11, v11, v12, v9
	v_med3_i32 v8, v12, v8, v9
	v_and_or_b32 v9, v128, s26, 24
	v_max_i32_e32 v12, v10, v9
	v_med3_i32 v10, v10, v11, v9
	v_med3_i32 v8, v11, v8, v9
	v_and_or_b32 v9, v129, s26, 25
	v_max_i32_e32 v11, v12, v9
	v_med3_i32 v12, v12, v10, v9
	v_med3_i32 v8, v10, v8, v9
	v_and_or_b32 v9, v130, s26, 26
	v_max_i32_e32 v10, v11, v9
	v_med3_i32 v11, v11, v12, v9
	v_med3_i32 v8, v12, v8, v9
	v_and_or_b32 v9, v131, s26, 27
	v_max_i32_e32 v12, v10, v9
	v_med3_i32 v10, v10, v11, v9
	v_med3_i32 v8, v11, v8, v9
	v_and_or_b32 v9, v120, s26, 28
	v_max_i32_e32 v11, v12, v9
	v_med3_i32 v12, v12, v10, v9
	v_med3_i32 v8, v10, v8, v9
	v_and_or_b32 v9, v121, s26, 29
	v_mov_b32_e32 v2, v0
	v_max_i32_e32 v10, v11, v9
	v_med3_i32 v11, v11, v12, v9
	v_med3_i32 v8, v12, v8, v9
	v_and_or_b32 v9, v122, s26, 30
	v_max_i32_e32 v12, v10, v9
	v_bfe_u32 v4, v2, 4, 2
	v_med3_i32 v10, v10, v11, v9
	v_med3_i32 v8, v11, v8, v9
	v_and_or_b32 v9, v123, s26, 31
	v_lshlrev_b32_e32 v7, 5, v4
	v_med3_i32 v8, v10, v8, v9
	v_max_i32_e32 v11, v12, v9
	v_med3_i32 v12, v12, v10, v9
	v_or_b32_e32 v38, v8, v7
	v_and_b32_e32 v8, 0xffffff80, v148
	v_and_or_b32 v9, v149, s26, 1
	v_or_b32_e32 v36, v11, v7
	v_or_b32_e32 v37, v12, v7
	v_max_i32_e32 v10, v8, v9
	v_min_i32_e32 v11, v8, v9
	v_and_or_b32 v12, v150, s26, 2
	v_max_i32_e32 v10, v10, v12
	v_med3_i32 v8, v8, v9, v12
	v_min_i32_e32 v9, v11, v12
	v_and_or_b32 v11, v151, s26, 3
	v_max_i32_e32 v12, v10, v11
	v_med3_i32 v10, v10, v8, v11
	v_min_i32_e32 v8, v8, v11
	v_max_i32_e32 v8, v9, v8
	v_and_or_b32 v9, v140, s26, 4
	v_max_i32_e32 v11, v12, v9
	v_med3_i32 v12, v12, v10, v9
	v_med3_i32 v8, v10, v8, v9
	v_and_or_b32 v9, v141, s26, 5
	v_max_i32_e32 v10, v11, v9
	v_med3_i32 v11, v11, v12, v9
	v_med3_i32 v8, v12, v8, v9
	v_and_or_b32 v9, v142, s26, 6
	v_max_i32_e32 v12, v10, v9
	v_med3_i32 v10, v10, v11, v9
	v_med3_i32 v8, v11, v8, v9
	v_and_or_b32 v9, v143, s26, 7
	v_max_i32_e32 v11, v12, v9
	v_med3_i32 v12, v12, v10, v9
	v_med3_i32 v8, v10, v8, v9
	v_and_or_b32 v9, v132, s26, 8
	v_max_i32_e32 v10, v11, v9
	v_med3_i32 v11, v11, v12, v9
	v_med3_i32 v8, v12, v8, v9
	v_and_or_b32 v9, v133, s26, 9
	v_max_i32_e32 v12, v10, v9
	v_med3_i32 v10, v10, v11, v9
	v_med3_i32 v8, v11, v8, v9
	v_and_or_b32 v9, v134, s26, 10
	v_max_i32_e32 v11, v12, v9
	v_med3_i32 v12, v12, v10, v9
	v_med3_i32 v8, v10, v8, v9
	v_and_or_b32 v9, v135, s26, 11
	v_max_i32_e32 v10, v11, v9
	v_med3_i32 v11, v11, v12, v9
	v_med3_i32 v8, v12, v8, v9
	v_and_or_b32 v9, v124, s26, 12
	v_max_i32_e32 v12, v10, v9
	v_med3_i32 v10, v10, v11, v9
	v_med3_i32 v8, v11, v8, v9
	v_and_or_b32 v9, v125, s26, 13
	v_max_i32_e32 v11, v12, v9
	v_med3_i32 v12, v12, v10, v9
	v_med3_i32 v8, v10, v8, v9
	v_and_or_b32 v9, v126, s26, 14
	v_max_i32_e32 v10, v11, v9
	v_med3_i32 v11, v11, v12, v9
	v_med3_i32 v8, v12, v8, v9
	v_and_or_b32 v9, v127, s26, 15
	v_max_i32_e32 v12, v10, v9
	v_med3_i32 v10, v10, v11, v9
	v_med3_i32 v8, v11, v8, v9
	v_and_or_b32 v9, v116, s26, 16
	v_max_i32_e32 v11, v12, v9
	v_med3_i32 v12, v12, v10, v9
	v_med3_i32 v8, v10, v8, v9
	v_and_or_b32 v9, v117, s26, 17
	v_max_i32_e32 v10, v11, v9
	v_med3_i32 v11, v11, v12, v9
	v_med3_i32 v8, v12, v8, v9
	v_and_or_b32 v9, v118, s26, 18
	v_max_i32_e32 v12, v10, v9
	v_med3_i32 v10, v10, v11, v9
	v_med3_i32 v8, v11, v8, v9
	v_and_or_b32 v9, v119, s26, 19
	v_max_i32_e32 v11, v12, v9
	v_med3_i32 v12, v12, v10, v9
	v_med3_i32 v8, v10, v8, v9
	v_and_or_b32 v9, v108, s26, 20
	v_max_i32_e32 v10, v11, v9
	v_med3_i32 v11, v11, v12, v9
	v_med3_i32 v8, v12, v8, v9
	v_and_or_b32 v9, v109, s26, 21
	v_max_i32_e32 v12, v10, v9
	v_med3_i32 v10, v10, v11, v9
	v_med3_i32 v8, v11, v8, v9
	v_and_or_b32 v9, v110, s26, 22
	v_max_i32_e32 v11, v12, v9
	v_med3_i32 v12, v12, v10, v9
	v_med3_i32 v8, v10, v8, v9
	v_and_or_b32 v9, v111, s26, 23
	v_max_i32_e32 v10, v11, v9
	v_med3_i32 v11, v11, v12, v9
	v_med3_i32 v8, v12, v8, v9
	v_and_or_b32 v9, v104, s26, 24
	v_max_i32_e32 v12, v10, v9
	v_med3_i32 v10, v10, v11, v9
	v_med3_i32 v8, v11, v8, v9
	v_and_or_b32 v9, v105, s26, 25
	v_max_i32_e32 v11, v12, v9
	v_med3_i32 v12, v12, v10, v9
	v_med3_i32 v8, v10, v8, v9
	v_and_or_b32 v9, v106, s26, 26
	v_max_i32_e32 v10, v11, v9
	v_med3_i32 v11, v11, v12, v9
	v_med3_i32 v8, v12, v8, v9
	v_and_or_b32 v9, v107, s26, 27
	v_max_i32_e32 v12, v10, v9
	v_med3_i32 v10, v10, v11, v9
	v_med3_i32 v8, v11, v8, v9
	v_and_or_b32 v9, v96, s26, 28
	v_max_i32_e32 v11, v12, v9
	v_med3_i32 v12, v12, v10, v9
	v_med3_i32 v8, v10, v8, v9
	v_and_or_b32 v9, v97, s26, 29
	v_ashrrev_i32_e32 v3, 6, v2
	v_max_i32_e32 v10, v11, v9
	v_med3_i32 v11, v11, v12, v9
	v_med3_i32 v8, v12, v8, v9
	v_and_or_b32 v9, v98, s26, 30
	v_and_b32_e32 v6, 63, v2
	v_lshl_add_u32 v5, v3, 12, s25
	v_max_i32_e32 v12, v10, v9
	v_med3_i32 v10, v10, v11, v9
	v_med3_i32 v8, v11, v8, v9
	v_and_or_b32 v9, v99, s26, 31
	v_lshl_add_u32 v6, v6, 4, v5
	v_med3_i32 v8, v10, v8, v9
	ds_write_b128 v6, v[36:39]
	v_max_i32_e32 v11, v12, v9
	v_med3_i32 v12, v12, v10, v9
	v_or_b32_e32 v38, v8, v7
	v_and_b32_e32 v8, 0xffffff80, v112
	v_and_or_b32 v9, v113, s26, 1
	v_or_b32_e32 v36, v11, v7
	v_or_b32_e32 v37, v12, v7
	v_max_i32_e32 v10, v8, v9
	v_min_i32_e32 v11, v8, v9
	v_and_or_b32 v12, v114, s26, 2
	v_max_i32_e32 v10, v10, v12
	v_med3_i32 v8, v8, v9, v12
	v_min_i32_e32 v9, v11, v12
	v_and_or_b32 v11, v115, s26, 3
	v_max_i32_e32 v12, v10, v11
	v_med3_i32 v10, v10, v8, v11
	v_min_i32_e32 v8, v8, v11
	v_max_i32_e32 v8, v9, v8
	v_and_or_b32 v9, v100, s26, 4
	v_max_i32_e32 v11, v12, v9
	v_med3_i32 v12, v12, v10, v9
	v_med3_i32 v8, v10, v8, v9
	v_and_or_b32 v9, v101, s26, 5
	v_max_i32_e32 v10, v11, v9
	v_med3_i32 v11, v11, v12, v9
	v_med3_i32 v8, v12, v8, v9
	v_and_or_b32 v9, v102, s26, 6
	v_max_i32_e32 v12, v10, v9
	v_med3_i32 v10, v10, v11, v9
	v_med3_i32 v8, v11, v8, v9
	v_and_or_b32 v9, v103, s26, 7
	v_max_i32_e32 v11, v12, v9
	v_med3_i32 v12, v12, v10, v9
	v_med3_i32 v8, v10, v8, v9
	v_and_or_b32 v9, v92, s26, 8
	v_max_i32_e32 v10, v11, v9
	v_med3_i32 v11, v11, v12, v9
	v_med3_i32 v8, v12, v8, v9
	v_and_or_b32 v9, v93, s26, 9
	v_max_i32_e32 v12, v10, v9
	v_med3_i32 v10, v10, v11, v9
	v_med3_i32 v8, v11, v8, v9
	v_and_or_b32 v9, v94, s26, 10
	v_max_i32_e32 v11, v12, v9
	v_med3_i32 v12, v12, v10, v9
	v_med3_i32 v8, v10, v8, v9
	v_and_or_b32 v9, v95, s26, 11
	v_max_i32_e32 v10, v11, v9
	v_med3_i32 v11, v11, v12, v9
	v_med3_i32 v8, v12, v8, v9
	v_and_or_b32 v9, v88, s26, 12
	v_max_i32_e32 v12, v10, v9
	v_med3_i32 v10, v10, v11, v9
	v_med3_i32 v8, v11, v8, v9
	v_and_or_b32 v9, v89, s26, 13
	v_max_i32_e32 v11, v12, v9
	v_med3_i32 v12, v12, v10, v9
	v_med3_i32 v8, v10, v8, v9
	v_and_or_b32 v9, v90, s26, 14
	v_max_i32_e32 v10, v11, v9
	v_med3_i32 v11, v11, v12, v9
	v_med3_i32 v8, v12, v8, v9
	v_and_or_b32 v9, v91, s26, 15
	v_max_i32_e32 v12, v10, v9
	v_med3_i32 v10, v10, v11, v9
	v_med3_i32 v8, v11, v8, v9
	v_and_or_b32 v9, v80, s26, 16
	v_max_i32_e32 v11, v12, v9
	v_med3_i32 v12, v12, v10, v9
	v_med3_i32 v8, v10, v8, v9
	v_and_or_b32 v9, v81, s26, 17
	v_max_i32_e32 v10, v11, v9
	v_med3_i32 v11, v11, v12, v9
	v_med3_i32 v8, v12, v8, v9
	v_and_or_b32 v9, v82, s26, 18
	v_max_i32_e32 v12, v10, v9
	v_med3_i32 v10, v10, v11, v9
	v_med3_i32 v8, v11, v8, v9
	v_and_or_b32 v9, v83, s26, 19
	v_max_i32_e32 v11, v12, v9
	v_med3_i32 v12, v12, v10, v9
	v_med3_i32 v8, v10, v8, v9
	v_and_or_b32 v9, v72, s26, 20
	v_max_i32_e32 v10, v11, v9
	v_med3_i32 v11, v11, v12, v9
	v_med3_i32 v8, v12, v8, v9
	v_and_or_b32 v9, v73, s26, 21
	v_max_i32_e32 v12, v10, v9
	v_med3_i32 v10, v10, v11, v9
	v_med3_i32 v8, v11, v8, v9
	v_and_or_b32 v9, v74, s26, 22
	v_max_i32_e32 v11, v12, v9
	v_med3_i32 v12, v12, v10, v9
	v_med3_i32 v8, v10, v8, v9
	v_and_or_b32 v9, v75, s26, 23
	v_max_i32_e32 v10, v11, v9
	v_med3_i32 v11, v11, v12, v9
	v_med3_i32 v8, v12, v8, v9
	v_and_or_b32 v9, v64, s26, 24
	v_max_i32_e32 v12, v10, v9
	v_med3_i32 v10, v10, v11, v9
	v_med3_i32 v8, v11, v8, v9
	v_and_or_b32 v9, v65, s26, 25
	v_max_i32_e32 v11, v12, v9
	v_med3_i32 v12, v12, v10, v9
	v_med3_i32 v8, v10, v8, v9
	v_and_or_b32 v9, v66, s26, 26
	v_max_i32_e32 v10, v11, v9
	v_med3_i32 v11, v11, v12, v9
	v_med3_i32 v8, v12, v8, v9
	v_and_or_b32 v9, v67, s26, 27
	v_max_i32_e32 v12, v10, v9
	v_med3_i32 v10, v10, v11, v9
	v_med3_i32 v8, v11, v8, v9
	v_and_or_b32 v9, v56, s26, 28
	v_max_i32_e32 v11, v12, v9
	v_med3_i32 v12, v12, v10, v9
	v_med3_i32 v8, v10, v8, v9
	v_and_or_b32 v9, v57, s26, 29
	v_max_i32_e32 v10, v11, v9
	v_med3_i32 v11, v11, v12, v9
	v_med3_i32 v8, v12, v8, v9
	v_and_or_b32 v9, v58, s26, 30
	v_max_i32_e32 v12, v10, v9
	v_med3_i32 v10, v10, v11, v9
	v_med3_i32 v8, v11, v8, v9
	v_and_or_b32 v9, v59, s26, 31
	v_med3_i32 v8, v10, v8, v9
	ds_write_b128 v6, v[36:39] offset:1024
	s_waitcnt vmcnt(0)
	s_barrier
	s_and_b64 vcc, exec, s[10:11]
	s_cbranch_vccnz .Lmid_skip
	s_add_u32 s68, s68, 0x6000
	s_addc_u32 s69, s69, 0
	s_add_u32 s70, s70, 0x6000
	s_addc_u32 s71, s71, 0
	s_mov_b32 m0, s60
	s_nop 0
	global_load_lds_dwordx4 v228, s[68:69]
	s_mov_b32 m0, s61
	s_nop 0
	global_load_lds_dwordx4 v229, s[68:69]
	s_mov_b32 m0, s62
	s_nop 0
	global_load_lds_dwordx4 v230, s[68:69]
	s_mov_b32 m0, s63
	s_nop 0
	global_load_lds_dwordx4 v228, s[70:71]
	s_mov_b32 m0, s64
	s_nop 0
	global_load_lds_dwordx4 v229, s[70:71]
	s_mov_b32 m0, s65
	s_nop 0
	global_load_lds_dwordx4 v230, s[70:71]
.Lmid_skip:
	v_max_i32_e32 v11, v12, v9
	v_med3_i32 v12, v12, v10, v9
	v_or_b32_e32 v38, v8, v7
	v_and_b32_e32 v8, 0xffffff80, v84
	v_and_or_b32 v9, v85, s26, 1
	v_or_b32_e32 v36, v11, v7
	v_or_b32_e32 v37, v12, v7
	v_max_i32_e32 v10, v8, v9
	v_min_i32_e32 v11, v8, v9
	v_and_or_b32 v12, v86, s26, 2
	v_max_i32_e32 v10, v10, v12
	v_med3_i32 v8, v8, v9, v12
	v_min_i32_e32 v9, v11, v12
	v_and_or_b32 v11, v87, s26, 3
	v_max_i32_e32 v12, v10, v11
	v_med3_i32 v10, v10, v8, v11
	v_min_i32_e32 v8, v8, v11
	v_max_i32_e32 v8, v9, v8
	v_and_or_b32 v9, v76, s26, 4
	v_max_i32_e32 v11, v12, v9
	v_med3_i32 v12, v12, v10, v9
	v_med3_i32 v8, v10, v8, v9
	v_and_or_b32 v9, v77, s26, 5
	v_max_i32_e32 v10, v11, v9
	v_med3_i32 v11, v11, v12, v9
	v_med3_i32 v8, v12, v8, v9
	v_and_or_b32 v9, v78, s26, 6
	v_max_i32_e32 v12, v10, v9
	v_med3_i32 v10, v10, v11, v9
	v_med3_i32 v8, v11, v8, v9
	v_and_or_b32 v9, v79, s26, 7
	v_max_i32_e32 v11, v12, v9
	v_med3_i32 v12, v12, v10, v9
	v_med3_i32 v8, v10, v8, v9
	v_and_or_b32 v9, v68, s26, 8
	v_max_i32_e32 v10, v11, v9
	v_med3_i32 v11, v11, v12, v9
	v_med3_i32 v8, v12, v8, v9
	v_and_or_b32 v9, v69, s26, 9
	v_max_i32_e32 v12, v10, v9
	v_med3_i32 v10, v10, v11, v9
	v_med3_i32 v8, v11, v8, v9
	v_and_or_b32 v9, v70, s26, 10
	v_max_i32_e32 v11, v12, v9
	v_med3_i32 v12, v12, v10, v9
	v_med3_i32 v8, v10, v8, v9
	v_and_or_b32 v9, v71, s26, 11
	v_max_i32_e32 v10, v11, v9
	v_med3_i32 v11, v11, v12, v9
	v_med3_i32 v8, v12, v8, v9
	v_and_or_b32 v9, v60, s26, 12
	v_max_i32_e32 v12, v10, v9
	v_med3_i32 v10, v10, v11, v9
	v_med3_i32 v8, v11, v8, v9
	v_and_or_b32 v9, v61, s26, 13
	v_max_i32_e32 v11, v12, v9
	v_med3_i32 v12, v12, v10, v9
	v_med3_i32 v8, v10, v8, v9
	v_and_or_b32 v9, v62, s26, 14
	v_max_i32_e32 v10, v11, v9
	v_med3_i32 v11, v11, v12, v9
	v_med3_i32 v8, v12, v8, v9
	v_and_or_b32 v9, v63, s26, 15
	v_max_i32_e32 v12, v10, v9
	v_med3_i32 v10, v10, v11, v9
	v_med3_i32 v8, v11, v8, v9
	v_and_or_b32 v9, v52, s26, 16
	v_max_i32_e32 v11, v12, v9
	v_med3_i32 v12, v12, v10, v9
	v_med3_i32 v8, v10, v8, v9
	v_and_or_b32 v9, v53, s26, 17
	v_max_i32_e32 v10, v11, v9
	v_med3_i32 v11, v11, v12, v9
	v_med3_i32 v8, v12, v8, v9
	v_and_or_b32 v9, v54, s26, 18
	v_max_i32_e32 v12, v10, v9
	v_med3_i32 v10, v10, v11, v9
	v_med3_i32 v8, v11, v8, v9
	v_and_or_b32 v9, v55, s26, 19
	v_max_i32_e32 v11, v12, v9
	v_med3_i32 v12, v12, v10, v9
	v_med3_i32 v8, v10, v8, v9
	v_and_or_b32 v9, v48, s26, 20
	v_max_i32_e32 v10, v11, v9
	v_med3_i32 v11, v11, v12, v9
	v_med3_i32 v8, v12, v8, v9
	v_and_or_b32 v9, v49, s26, 21
	v_max_i32_e32 v12, v10, v9
	v_med3_i32 v10, v10, v11, v9
	v_med3_i32 v8, v11, v8, v9
	v_and_or_b32 v9, v50, s26, 22
	v_max_i32_e32 v11, v12, v9
	v_med3_i32 v12, v12, v10, v9
	v_med3_i32 v8, v10, v8, v9
	v_and_or_b32 v9, v51, s26, 23
	v_max_i32_e32 v10, v11, v9
	v_med3_i32 v11, v11, v12, v9
	v_med3_i32 v8, v12, v8, v9
	v_and_or_b32 v9, v44, s26, 24
	v_max_i32_e32 v12, v10, v9
	v_med3_i32 v10, v10, v11, v9
	v_med3_i32 v8, v11, v8, v9
	v_and_or_b32 v9, v45, s26, 25
	v_max_i32_e32 v11, v12, v9
	v_med3_i32 v12, v12, v10, v9
	v_med3_i32 v8, v10, v8, v9
	v_and_or_b32 v9, v46, s26, 26
	v_max_i32_e32 v10, v11, v9
	v_med3_i32 v11, v11, v12, v9
	v_med3_i32 v8, v12, v8, v9
	v_and_or_b32 v9, v47, s26, 27
	v_max_i32_e32 v12, v10, v9
	v_med3_i32 v10, v10, v11, v9
	v_med3_i32 v8, v11, v8, v9
	v_and_or_b32 v9, v40, s26, 28
	v_max_i32_e32 v11, v12, v9
	v_med3_i32 v12, v12, v10, v9
	v_med3_i32 v8, v10, v8, v9
	v_and_or_b32 v9, v41, s26, 29
	v_max_i32_e32 v10, v11, v9
	v_med3_i32 v11, v11, v12, v9
	v_med3_i32 v8, v12, v8, v9
	v_and_or_b32 v9, v42, s26, 30
	v_max_i32_e32 v12, v10, v9
	v_med3_i32 v10, v10, v11, v9
	v_med3_i32 v8, v11, v8, v9
	v_and_or_b32 v9, v43, s26, 31
	v_max_i32_e32 v11, v12, v9
	v_med3_i32 v12, v12, v10, v9
	v_med3_i32 v8, v10, v8, v9
	ds_write_b128 v6, v[36:39] offset:2048
	v_or_b32_e32 v36, v11, v7
	v_or_b32_e32 v37, v12, v7
	v_or_b32_e32 v38, v8, v7
	v_and_b32_e32 v23, 15, v2
	ds_write_b128 v6, v[36:39] offset:3072
	v_lshlrev_b32_e32 v4, 10, v4
	v_lshlrev_b32_e32 v6, 4, v23
	s_waitcnt lgkmcnt(0)
	v_add3_u32 v16, v5, v4, v6
	ds_read_b128 v[4:7], v16
	ds_read_b128 v[8:11], v16 offset:256
	ds_read_b128 v[12:15], v16 offset:512
	ds_read_b128 v[16:19], v16 offset:768
	v_lshlrev_b32_e32 v3, 5, v3
	s_lshl_b32 s34, s34, 8
	v_ashrrev_i32_e32 v24, 8, v2
	s_waitcnt lgkmcnt(0)
	v_max_i32_e32 v7, v4, v5
	v_min_i32_e32 v11, v4, v5
	v_max_i32_e32 v7, v7, v6
	v_med3_i32 v4, v4, v5, v6
	v_min_i32_e32 v5, v11, v6
	v_max_i32_e32 v11, v7, v8
	v_med3_i32 v7, v7, v4, v8
	v_min_i32_e32 v4, v4, v8
	v_max_i32_e32 v4, v5, v4
	v_min_i32_e32 v5, v5, v8
	v_max_i32_e32 v8, v11, v9
	v_med3_i32 v11, v11, v7, v9
	v_med3_i32 v7, v7, v4, v9
	v_min_i32_e32 v4, v4, v9
	v_max_i32_e32 v4, v5, v4
	v_max_i32_e32 v5, v8, v10
	v_med3_i32 v8, v8, v11, v10
	v_med3_i32 v9, v11, v7, v10
	v_med3_i32 v4, v7, v4, v10
	v_max_i32_e32 v7, v5, v12
	v_med3_i32 v5, v5, v8, v12
	v_med3_i32 v8, v8, v9, v12
	v_med3_i32 v4, v9, v4, v12
	v_max_i32_e32 v9, v7, v13
	v_med3_i32 v7, v7, v5, v13
	v_med3_i32 v5, v5, v8, v13
	v_med3_i32 v4, v8, v4, v13
	v_max_i32_e32 v8, v9, v14
	v_med3_i32 v9, v9, v7, v14
	v_med3_i32 v7, v7, v5, v14
	v_med3_i32 v4, v5, v4, v14
	v_max_i32_e32 v5, v8, v16
	v_med3_i32 v8, v8, v9, v16
	v_med3_i32 v9, v9, v7, v16
	v_med3_i32 v4, v7, v4, v16
	v_max_i32_e32 v7, v5, v17
	v_med3_i32 v5, v5, v8, v17
	v_max_i32_e32 v20, v7, v18
	v_med3_i32 v21, v7, v5, v18
	v_max_i32_e32 v7, v14, v18
	v_max3_i32 v6, v6, v10, v7
	v_lshlrev_b32_e32 v7, 2, v2
	v_and_b32_e32 v3, 0x60, v3
	v_and_b32_e32 v2, 16, v2
	s_lshl_b32 s36, s13, 1
	v_med3_i32 v8, v8, v9, v17
	v_med3_i32 v4, v9, v4, v17
	v_and_b32_e32 v7, 0x80, v7
	v_or3_b32 v2, v2, s34, v3
	s_ashr_i32 s37, s36, 31
	v_ashrrev_i32_e32 v25, 31, v24
	v_med3_i32 v22, v5, v8, v18
	v_min_i32_e32 v5, v8, v4
	v_max_i32_e32 v4, v8, v4
	v_or3_b32 v7, v2, v7, v23
	v_lshl_add_u64 v[2:3], v[24:25], 0, s[36:37]
	v_min_i32_e32 v4, v4, v18
	v_mad_i64_i32 v[2:3], s[36:37], v7, s27, v[2:3]
	v_max3_i32 v23, v5, v4, v6
	v_lshl_add_u64 v[2:3], v[2:3], 4, s[8:9]
	s_andn2_b64 vcc, exec, s[10:11]
	s_mov_b32 s13, s3
	s_mov_b32 s34, s35
	global_store_dwordx4 v[2:3], v[20:23], off
	s_cbranch_vccz .LBB1_8
.LBB1_2:
	s_mul_i32 s41, s34, 0x30000
	s_mul_hi_i32 s40, s34, 0x30000
	s_add_u32 s11, s6, s41
	s_addc_u32 s35, s7, s40
	s_mov_b32 s10, s2
	s_add_u32 s2, s11, 0x6000
	s_addc_u32 s3, s35, 0
	s_mul_i32 s43, s13, 0x30000
	s_mul_hi_i32 s42, s13, 0x30000
	s_add_u32 s44, s4, s43
	s_addc_u32 s45, s5, s42
	s_add_u32 s38, s11, 0x8000
	s_addc_u32 s39, s35, 0
	s_add_u32 s46, s44, 0x5000
	s_addc_u32 s47, s45, 0
	s_and_b64 s[36:37], s[0:1], exec
	s_cselect_b32 s37, s39, s47
	s_cselect_b32 s36, s38, s46
	s_add_u32 s38, s44, 0x7000
	s_addc_u32 s39, s45, 0
	s_add_u32 s2, s11, 0x9000
	s_addc_u32 s3, s35, 0
	s_add_u32 s11, s11, 0xb000
	s_addc_u32 s35, s35, 0
	s_add_u32 s38, s44, 0x8000
	s_addc_u32 s39, s45, 0
	s_and_b64 s[36:37], s[0:1], exec
	s_cselect_b32 s37, s35, s39
	s_cselect_b32 s36, s11, s38
	s_add_u32 s38, s44, 0xa000
	s_addc_u32 s39, s45, 0
	s_add_u32 s11, s21, s43
	s_addc_u32 s35, s22, s42
	ds_read_b128 v[2:5], v170 offset:12288
	ds_read_b64 v[6:7], v173 offset:12352
	ds_read_b128 v[8:11], v170 offset:13824
	ds_read_b64 v[12:13], v173 offset:13888
	ds_read_b128 v[14:17], v170 offset:15360
	ds_read_b64 v[18:19], v173 offset:15424
	ds_read_b128 v[26:29], v170 offset:16896
	ds_read_b64 v[30:31], v173 offset:16960
	ds_read_b128 v[20:23], v1
	ds_read_b64 v[24:25], v172 offset:64
	ds_read_b128 v[32:35], v1 offset:1536
	ds_read_b64 v[36:37], v172 offset:1600
	s_add_u32 s2, s23, s41
	s_addc_u32 s3, s24, s40
	s_mov_b32 s36, -2
	s_waitcnt lgkmcnt(0)
